# differential-attention tile loop: K-fragment LDS address lane parts hoisted out of the tile loop, first fragment reads issued before the score-accumulator bias initialisation
# speedup vs baseline: 1.0066x; 1.0005x over previous
; #define LAS __attribute__((address_space(3)))
; __device__ __forceinline__ void attn_unit_da(const bf16_t* QKV, bf16_t* O, int b, int h, int qb, float slope2, int dmax, bool freeze_ok, const float* const* in, float lambda_init, LAS char* lds) {
;     ...
;               const LAS char* Ks = lds + bf * STG + c * SHM_T; int ln_ = lane; asm volatile("" : "+v"(ln_)); const int r32_ = ln_ & 31, hi_ = ln_ >> 5;
;               const LAS char* kb0 = Ks + (r32_ * 256 + (((0 * 2 + hi_) ^ (r32_ & 7)) << 4)); const LAS char* kb1 = Ks + (r32_ * 256 + (((1 * 2 + hi_) ^ (r32_ & 7)) << 4));
;               const LAS char* kb2 = Ks + (r32_ * 256 + (((2 * 2 + hi_) ^ (r32_ & 7)) << 4)); const LAS char* kb3 = Ks + (r32_ * 256 + (((3 * 2 + hi_) ^ (r32_ & 7)) << 4));
; __device__ __forceinline__ void attn_phase_da(const Frame& F, const Args& a) {
;     const float* qn = a.in[8]; const float* kn = a.in[9];
;     float gq = fmaxf(fabsf(qn[F.lane]), fabsf(qn[F.lane + 64])), gk = fmaxf(fabsf(kn[F.lane]), fabsf(kn[F.lane + 64]));
; #pragma unroll
;     for (int o = 1; o < 64; o <<= 1) { gq = fmaxf(gq, __shfl_xor(gq, o)); gk = fmaxf(gk, __shfl_xor(gk, o)); }
;     const float zb2 = 128.f * gq * gk * 1.01f * att::QK_C;
;     const float lambda_init = 0.8f - 0.6f * 0.7408182206817179f;
.LBB0_1122:
	s_cmp_gt_i32 s8, 17
	s_cselect_b64 s[0:1], -1, 0
	s_cmp_lt_i32 s9, 18
	s_cselect_b64 s[2:3], -1, 0
	s_or_b64 s[0:1], s[0:1], s[2:3]
	s_and_b64 vcc, exec, s[0:1]
	s_cbranch_vccnz .LBB0_1204
	v_lshlrev_b32_e32 v1, 2, v230
	global_load_dword v4, v1, s[76:77] offset:256
	global_load_dword v2, v1, s[76:77]
	global_load_dword v6, v1, s[78:79] offset:256
	global_load_dword v5, v1, s[78:79]
	s_waitcnt vmcnt(0)
	v_mbcnt_lo_u32_b32 v7, -1, 0
	v_lshlrev_b32_e32 v11, 4, v0
	v_mbcnt_hi_u32_b32 v7, -1, v7
	v_lshlrev_b32_e32 v9, 1, v0
	v_and_b32_e32 v11, 0xc0, v11
	v_and_b32_e32 v12, 64, v7
	v_xor_b32_e32 v13, 1, v7
	v_and_or_b32 v9, v9, 32, v11
	v_add_u32_e32 v11, 64, v12
	v_cmp_lt_i32_e32 vcc, v13, v11
	v_xor_b32_e32 v14, 2, v7
	v_xor_b32_e32 v15, 4, v7
	v_cndmask_b32_e32 v12, v7, v13, vcc
	v_lshlrev_b32_e32 v228, 2, v12
	v_cmp_lt_i32_e32 vcc, v14, v11
	v_xor_b32_e32 v16, 8, v7
	v_xor_b32_e32 v17, 16, v7
	v_cndmask_b32_e32 v12, v7, v14, vcc
	v_lshlrev_b32_e32 v229, 2, v12
	v_cmp_lt_i32_e32 vcc, v15, v11
	v_xor_b32_e32 v18, 32, v7
	s_add_i32 s0, 0, 0x8000
	v_cndmask_b32_e32 v12, v7, v15, vcc
	v_lshlrev_b32_e32 v232, 2, v12
	v_cmp_lt_i32_e32 vcc, v16, v11
	v_writelane_b32 v255, s92, 47
	v_lshrrev_b32_e32 v227, 5, v230
	v_cndmask_b32_e32 v12, v7, v16, vcc
	v_lshlrev_b32_e32 v233, 2, v12
	v_cmp_lt_i32_e32 vcc, v17, v11
	v_lshlrev_b32_e32 v10, 3, v0
	s_add_u32 s1, s90, 0x49a01000
	v_cndmask_b32_e32 v12, v7, v17, vcc
	v_lshlrev_b32_e32 v234, 2, v12
	v_cmp_lt_i32_e32 vcc, v18, v11
	v_mov_b32_e32 v1, 0x43160000
	s_mov_b32 s16, 2.0
	v_cndmask_b32_e32 v7, v7, v18, vcc
	v_lshlrev_b32_e32 v235, 2, v7
	s_mov_b32 s18, 0x41000000
	s_mov_b32 s20, 0x41200000
	s_mov_b32 s22, 0x41800000
	s_mov_b32 s24, 0x41900000
	s_mov_b32 s26, 0x41c00000
	s_mov_b32 s28, 0x41d00000
	s_mov_b32 s30, 0x42680000
	s_mov_b32 s34, 0x42600000
	s_mov_b32 s36, 0x42480000
	s_mov_b32 s40, 0x42400000
	s_mov_b32 s42, 0x42280000
	v_lshlrev_b32_e32 v8, 3, v227
	v_and_b32_e32 v10, 0x118, v10
	v_writelane_b32 v255, s1, 48
	s_addc_u32 s1, s91, 0
	s_add_i32 s75, 0, 0x21800
	s_mov_b32 s46, 0x42200000
	s_mov_b32 s48, 0x42080000
	s_mov_b32 s50, 0x42000000
	s_mov_b32 s67, 0
	s_mov_b32 s17, 0x40400000
	v_and_b32_e32 v226, 31, v0
	v_mov_b32_e32 v3, 0
	s_movk_i32 s79, 0x1800
	s_movk_i32 s45, 0x70
	s_mov_b64 s[88:89], 0x1000
	s_mov_b64 s[38:39], 0x100
	s_mov_b64 s[84:85], 0x1100
	s_mov_b32 s19, 0x41100000
	s_mov_b32 s21, 0x41300000
	s_mov_b32 s23, 0x41880000
	s_mov_b32 s25, 0x41980000
	s_mov_b32 s27, 0x41c80000
	s_mov_b32 s29, 0x41d80000
	s_mov_b32 s31, 0x426c0000
	s_mov_b32 s35, 0x42640000
	s_mov_b32 s37, 0x424c0000
	v_max_f32_e64 v4, |v4|, |v4|
	v_max_f32_e64 v2, |v2|, |v2|
	v_max_f32_e64 v6, |v6|, |v6|
	v_max_f32_e64 v5, |v5|, |v5|
	v_max_f32_e32 v2, v2, v4
	v_max_f32_e32 v4, v5, v6
	ds_bpermute_b32 v5, v228, v2
	ds_bpermute_b32 v6, v228, v4
	s_mov_b32 s41, 0x42440000
	s_mov_b32 s43, 0x422c0000
	v_writelane_b32 v255, s1, 49
	s_waitcnt lgkmcnt(1)
	v_max_f32_e32 v5, v5, v5
	s_waitcnt lgkmcnt(0)
	v_max_f32_e32 v6, v6, v6
	v_max_f32_e32 v2, v2, v5
	v_max_f32_e32 v4, v4, v6
	ds_bpermute_b32 v5, v229, v2
	ds_bpermute_b32 v6, v229, v4
	v_lshlrev_b32_e32 v210, 1, v8
	v_add3_u32 v236, v10, s0, v9
	v_mov_b32_e32 v237, s75
	s_waitcnt lgkmcnt(1)
	v_max_f32_e32 v5, v5, v5
	s_waitcnt lgkmcnt(0)
	v_max_f32_e32 v6, v6, v6
	v_max_f32_e32 v2, v2, v5
	v_max_f32_e32 v4, v4, v6
	ds_bpermute_b32 v5, v232, v2
	ds_bpermute_b32 v6, v232, v4
	s_mov_b32 s47, 0x42240000
	s_mov_b32 s49, 0x420c0000
	s_mov_b32 s51, 0x42040000
	s_waitcnt lgkmcnt(1)
	v_max_f32_e32 v5, v5, v5
	s_waitcnt lgkmcnt(0)
	v_max_f32_e32 v6, v6, v6
	v_max_f32_e32 v2, v2, v5
	v_max_f32_e32 v4, v4, v6
	ds_bpermute_b32 v5, v233, v2
	ds_bpermute_b32 v6, v233, v4
	s_mov_b32 s95, 0xc3e00000
	v_mov_b32_e32 v238, 0x42800000
	v_mov_b32_e32 v239, 0xf4240
	s_waitcnt lgkmcnt(1)
	v_max_f32_e32 v5, v5, v5
	s_waitcnt lgkmcnt(0)
	v_max_f32_e32 v6, v6, v6
	v_max_f32_e32 v2, v2, v5
	v_max_f32_e32 v4, v4, v6
	ds_bpermute_b32 v5, v234, v2
	ds_bpermute_b32 v6, v234, v4
	v_mov_b32_e32 v240, 0xff800000
	v_mov_b32_e32 v241, 0x43e00000
	s_waitcnt lgkmcnt(1)
	v_max_f32_e32 v5, v5, v5
	s_waitcnt lgkmcnt(0)
	v_max_f32_e32 v6, v6, v6
	v_max_f32_e32 v2, v2, v5
	v_max_f32_e32 v4, v4, v6
	ds_bpermute_b32 v5, v235, v2
	ds_bpermute_b32 v6, v235, v4
	s_waitcnt lgkmcnt(1)
	v_max_f32_e32 v5, v5, v5
	s_waitcnt lgkmcnt(0)
	v_max_f32_e32 v6, v6, v6
	v_max_f32_e32 v2, v2, v5
	v_max_f32_e32 v4, v4, v6
	v_mul_f32_e32 v2, 0x43000000, v2
	v_mul_f32_e32 v2, v4, v2
	v_mul_f32_e32 v2, 0x3f8147ae, v2
	v_mul_f32_e32 v2, 0x3e0293ee, v2
	v_fmac_f32_e32 v1, 2.0, v2
	v_lshlrev_b32_e32 v8, 8, v230
	v_ashrrev_i32_e32 v7, 5, v230
	v_and_b32_e32 v8, 0x1f00, v8
	v_bitop3_b32 v9, v7, v230, 7 bitop3:0x78
	v_lshl_add_u32 v252, v9, 4, v8
	v_add_u32_e32 v9, 2, v7
	v_bitop3_b32 v9, v9, v230, 7 bitop3:0x78
	v_lshl_add_u32 v253, v9, 4, v8
	v_add_u32_e32 v9, 4, v7
	v_bitop3_b32 v9, v9, v230, 7 bitop3:0x78
	v_lshl_add_u32 v254, v9, 4, v8
	s_branch .LBB0_1126

; #define LAS __attribute__((address_space(3)))
; #define QKRD(S, KB, OFF) do { S##0 = *(const LAS bf16x8*)((KB) + (OFF)); S##1 = *(const LAS bf16x8*)((KB) + (OFF) + 8192); } while (0)
; __device__ __forceinline__ void attn_unit_da(const bf16_t* QKV, bf16_t* O, int b, int h, int qb, float slope2, int dmax, bool freeze_ok, const float* const* in, float lambda_init, LAS char* lds) {
;     ...
;     for (int it = 0; it < NIT; ++it) {
;         const int k0 = (NT - 1 - it) * KVBLK, bf = it & 1;
;         asm volatile("s_waitcnt vmcnt(0)" ::: "memory");
;         __syncthreads();
;         if (it + 1 < NIT) DMA_DA((NT - 2 - it) * KVBLK, bf ^ 1);
;         const bool active = (k0 <= r0) && (k0 + 63 + dmax >= r0);
;         if (active) {
;             int lt_ = lane; asm volatile("" : "+v"(lt_)); const int hi_t = lt_ >> 5, r32_t = lt_ & 31;
;             const float fb = slope2 * (float)(k0 - r0 + 4 * hi_t);
;             const bool need_mask = (k0 + 63 > r0);
;             const float cb = fb;
;             f32x16 p0, p1; float sl_ = slope2; asm volatile("" : "+v"(sl_));
; #pragma unroll
;             for (int r = 0; r < 16; ++r) { p0[r] = fmaf(sl_, (float)((r & 3) + 8 * (r >> 2)), cb); p1[r] = fmaf(sl_, (float)(32 + (r & 3) + 8 * (r >> 2)), cb); }
;             {
;               const LAS char* Ks = lds + bf * STG + c * SHM_T; int ln_ = lane; asm volatile("" : "+v"(ln_)); const int r32_ = ln_ & 31, hi_ = ln_ >> 5;
;               const LAS char* kb0 = Ks + (r32_ * 256 + (((0 * 2 + hi_) ^ (r32_ & 7)) << 4)); const LAS char* kb1 = Ks + (r32_ * 256 + (((1 * 2 + hi_) ^ (r32_ & 7)) << 4));
;               const LAS char* kb2 = Ks + (r32_ * 256 + (((2 * 2 + hi_) ^ (r32_ & 7)) << 4)); const LAS char* kb3 = Ks + (r32_ * 256 + (((3 * 2 + hi_) ^ (r32_ & 7)) << 4));
;               bf16x8 xa0, xa1, xb0, xb1;
;     ...
;               QKRD(xa, kb0, 0);
;               QKRD(xb, kb0, 128); QKMM(xa, 0, 2);
;               QKRD(xa, kb1, 0);   QKMM(xb, 4, 2);
;               QKRD(xb, kb1, 128); QKMM(xa, 1, 2);
;               QKRD(xa, kb2, 0);   QKMM(xb, 5, 2);
;               QKRD(xb, kb2, 128); QKMM(xa, 2, 2);
;               QKRD(xa, kb3, 0);   QKMM(xb, 6, 2);
;               QKRD(xb, kb3, 128); QKMM(xa, 3, 2);
;                                   QKMM(xb, 7, 0);
.LBB0_1136:
	s_waitcnt vmcnt(0)
	s_add_i32 s0, s86, -1
	s_and_b32 s8, s0, 1
	v_cmp_ge_i32_e64 s[0:1], s86, v211
	s_waitcnt vmcnt(0) lgkmcnt(0)
	s_barrier
	s_sub_i32 s6, s80, 63
	s_cmp_le_i32 s6, s69
	v_add_u32_e32 v2, s80, v213
	s_cselect_b64 s[6:7], -1, 0
	v_cmp_le_i32_e32 vcc, s69, v2
	s_and_b64 s[6:7], s[6:7], vcc
	s_and_saveexec_b64 s[76:77], s[6:7]
	s_cbranch_execz .Lda_inactive
	s_lshl_b32 s99, s8, 16
	s_lshl_b32 s94, s8, 16
	s_xor_b32 s99, s99, 0x10000
	s_add_i32 s6, s96, s94
	s_add_i32 s99, s91, s99
	v_xor_b32_e32 v2, 64, v253
	v_add_u32_e32 v16, s6, v252
	v_add_u32_e32 v17, s6, v253
	v_add_u32_e32 v224, s6, v254
	v_add_u32_e32 v2, s6, v2
	ds_read_b128 v[8:11], v16
	ds_read_b128 v[12:15], v16 offset:128
	ds_read_b128 v[216:219], v16 offset:8192
	ds_read_b128 v[220:223], v16 offset:8320
	v_ashrrev_i32_e32 v5, 3, v230
	v_and_b32_e32 v4, -4, v5
	v_add_u32_e32 v5, s97, v4
	v_cvt_f32_i32_e32 v7, v5
	v_mul_f32_e32 v6, v212, v7
	v_subrev_f32_e32 v6, s98, v6
	v_fma_f32 v146, 0, v212, v6
	v_pk_fma_f32 v[148:149], v[212:213], s[16:17], v[6:7] op_sel_hi:[0,1,0]
	v_pk_fma_f32 v[150:151], v[212:213], s[18:19], v[6:7] op_sel_hi:[0,1,0]
	v_pk_fma_f32 v[152:153], v[212:213], s[20:21], v[6:7] op_sel_hi:[0,1,0]
	v_pk_fma_f32 v[154:155], v[212:213], s[22:23], v[6:7] op_sel_hi:[0,1,0]
	v_pk_fma_f32 v[156:157], v[212:213], s[24:25], v[6:7] op_sel_hi:[0,1,0]
	v_pk_fma_f32 v[158:159], v[212:213], s[26:27], v[6:7] op_sel_hi:[0,1,0]
	v_pk_fma_f32 v[160:161], v[212:213], s[28:29], v[6:7] op_sel_hi:[0,1,0]
	v_pk_fma_f32 v[176:177], v[212:213], s[30:31], v[6:7] op_sel_hi:[0,1,0]
	v_pk_fma_f32 v[174:175], v[212:213], s[34:35], v[6:7] op_sel_hi:[0,1,0]
	v_pk_fma_f32 v[172:173], v[212:213], s[36:37], v[6:7] op_sel_hi:[0,1,0]
	v_pk_fma_f32 v[170:171], v[212:213], s[40:41], v[6:7] op_sel_hi:[0,1,0]
	v_pk_fma_f32 v[168:169], v[212:213], s[42:43], v[6:7] op_sel_hi:[0,1,0]
	v_pk_fma_f32 v[166:167], v[212:213], s[46:47], v[6:7] op_sel_hi:[0,1,0]
	v_pk_fma_f32 v[164:165], v[212:213], s[48:49], v[6:7] op_sel_hi:[0,1,0]
	v_pk_fma_f32 v[162:163], v[212:213], s[50:51], v[6:7] op_sel_hi:[0,1,0]
	v_add_f32_e32 v147, v212, v6
	s_waitcnt lgkmcnt(2)
	v_and_b32_e32 v6, 31, v230
	s_waitcnt lgkmcnt(0)
	v_mfma_f32_32x32x16_bf16 v[146:161], v[8:11], v[178:181], v[146:161]
	v_mfma_f32_32x32x16_bf16 v[162:177], v[216:219], v[178:181], v[162:177]
	ds_read_b128 v[8:11], v17
	ds_read_b128 v[216:219], v17 offset:8192
	s_mov_b32 m0, s99
	s_add_u32 s100, s72, 0x0
	s_addc_u32 s101, s73, 0
	global_load_lds_dwordx4 v250, s[100:101]
	s_waitcnt lgkmcnt(2)
	v_mfma_f32_32x32x16_bf16 v[146:161], v[12:15], v[194:197], v[146:161]
	v_mfma_f32_32x32x16_bf16 v[162:177], v[220:223], v[194:197], v[162:177]
	ds_read_b128 v[12:15], v17 offset:128
	ds_read_b128 v[220:223], v17 offset:8320
	s_add_i32 m0, s99, 0x4000
	s_add_u32 s100, s72, 0x100
	s_addc_u32 s101, s73, 0
	global_load_lds_dwordx4 v250, s[100:101]
	s_waitcnt lgkmcnt(2)
	s_waitcnt lgkmcnt(0)
	v_mfma_f32_32x32x16_bf16 v[146:161], v[8:11], v[182:185], v[146:161]
	v_mfma_f32_32x32x16_bf16 v[162:177], v[216:219], v[182:185], v[162:177]
	ds_read_b128 v[8:11], v224
	ds_read_b128 v[216:219], v224 offset:8192
	s_add_i32 m0, s99, 0x2000
	s_add_u32 s100, s72, 0x60000
	s_addc_u32 s101, s73, 0
	global_load_lds_dwordx4 v250, s[100:101]
	s_waitcnt lgkmcnt(2)
	v_mfma_f32_32x32x16_bf16 v[146:161], v[12:15], v[198:201], v[146:161]
	v_mfma_f32_32x32x16_bf16 v[162:177], v[220:223], v[198:201], v[162:177]
	ds_read_b128 v[12:15], v224 offset:128
	ds_read_b128 v[220:223], v224 offset:8320
	s_add_i32 m0, s99, 0x6000
	s_add_u32 s100, s72, 0x60100
	s_addc_u32 s101, s73, 0
	global_load_lds_dwordx4 v250, s[100:101]
	s_waitcnt lgkmcnt(2)
	s_waitcnt lgkmcnt(0)
	v_mfma_f32_32x32x16_bf16 v[146:161], v[8:11], v[186:189], v[146:161]
	v_mfma_f32_32x32x16_bf16 v[162:177], v[216:219], v[186:189], v[162:177]
	ds_read_b128 v[8:11], v2
	ds_read_b128 v[216:219], v2 offset:8192
	s_add_i32 m0, s99, 0x8000
	s_add_u32 s100, s72, 0x1000
	s_addc_u32 s101, s73, 0
	global_load_lds_dwordx4 v251, s[100:101]
	s_waitcnt lgkmcnt(2)
	v_mfma_f32_32x32x16_bf16 v[146:161], v[12:15], v[202:205], v[146:161]
	v_mfma_f32_32x32x16_bf16 v[162:177], v[220:223], v[202:205], v[162:177]
	ds_read_b128 v[12:15], v2 offset:128
	ds_read_b128 v[220:223], v2 offset:8320
	s_add_i32 m0, s99, 0xc000
	s_add_u32 s100, s72, 0x1100
	s_addc_u32 s101, s73, 0
	global_load_lds_dwordx4 v251, s[100:101]
	s_waitcnt lgkmcnt(2)
	s_waitcnt lgkmcnt(0)
	v_mfma_f32_32x32x16_bf16 v[146:161], v[8:11], v[190:193], v[146:161]
	v_mfma_f32_32x32x16_bf16 v[162:177], v[216:219], v[190:193], v[162:177]
	s_add_i32 m0, s99, 0xa000
	s_add_u32 s100, s72, 0x61000
	s_addc_u32 s101, s73, 0
	global_load_lds_dwordx4 v251, s[100:101]
	s_waitcnt lgkmcnt(0)
	v_mfma_f32_32x32x16_bf16 v[146:161], v[12:15], v[206:209], v[146:161]
	v_mfma_f32_32x32x16_bf16 v[162:177], v[220:223], v[206:209], v[162:177]
	s_add_i32 m0, s99, 0xe000
	s_add_u32 s100, s72, 0x61100
	s_addc_u32 s101, s73, 0
	global_load_lds_dwordx4 v251, s[100:101]
	s_cmp_le_i32 s80, s69
	s_cbranch_scc1 .LBB0_1141
; __device__ __forceinline__ void attn_unit_da(const bf16_t* QKV, bf16_t* O, int b, int h, int qb, float slope2, int dmax, bool freeze_ok, const float* const* in, float lambda_init, LAS char* lds) {
;     ...
;                 if (need_mask) { const int kq = k0 - (r0 + r32_t) + 4 * hi_t;
; #pragma unroll
;                     for (int r = 0; r < 16; ++r) { const int kr = kq + (r & 3) + 8 * (r >> 2); if (kr > 0) p0[r] = -INFINITY; if (kr + 32 > 0) p1[r] = -INFINITY; } }
	v_sub_u32_e32 v2, v4, v6
	v_add_u32_e32 v2, s97, v2
	s_movk_i32 s34, 0xffe6
	s_movk_i32 s64, 0xffe5
	s_movk_i32 s30, 0xffe7
	v_cmp_lt_i32_e64 s[62:63], s34, v2
	v_cmp_lt_i32_e64 s[64:65], s64, v2
	s_movk_i32 s28, 0xffe8
	v_cmp_lt_i32_e64 s[60:61], s30, v2
	s_and_b64 s[62:63], s[64:65], s[62:63]
	s_movk_i32 s26, 0xffed
	v_cmp_lt_i32_e64 s[58:59], s28, v2
	s_and_b64 s[60:61], s[62:63], s[60:61]
	s_movk_i32 s24, 0xffee
	v_cmp_lt_i32_e64 s[56:57], s26, v2
	s_and_b64 s[58:59], s[60:61], s[58:59]
	s_movk_i32 s22, 0xffef
	v_cmp_lt_i32_e64 s[54:55], s24, v2
	s_and_b64 s[56:57], s[58:59], s[56:57]
	v_cmp_lt_i32_e64 s[52:53], s22, v2
	s_and_b64 s[54:55], s[56:57], s[54:55]
	v_cmp_lt_i32_e64 s[50:51], -16, v2
	s_and_b64 s[52:53], s[54:55], s[52:53]
	v_cmp_lt_i32_e64 s[48:49], -11, v2
	s_and_b64 s[50:51], s[52:53], s[50:51]
	v_cmp_lt_i32_e64 s[46:47], -10, v2
	s_and_b64 s[48:49], s[50:51], s[48:49]
	v_cmp_lt_i32_e64 s[44:45], -9, v2
	s_and_b64 s[46:47], s[48:49], s[46:47]
	s_movk_i32 s8, 0xffe0
	v_cmp_lt_i32_e64 s[42:43], -8, v2
	s_and_b64 s[44:45], s[46:47], s[44:45]
	v_cmp_gt_i32_e64 s[6:7], 1, v2
	v_cmp_lt_i32_e32 vcc, s8, v2
	v_cmp_gt_i32_e64 s[8:9], 0, v2
	v_cmp_lt_i32_e64 s[40:41], -3, v2
	s_and_b64 s[42:43], s[44:45], s[42:43]
	s_or_b64 s[6:7], s[8:9], s[6:7]
	v_cmp_lt_i32_e64 s[36:37], -2, v2
	s_and_b64 s[40:41], s[42:43], s[40:41]
	v_cndmask_b32_e64 v7, v240, v147, s[8:9]
	v_cndmask_b32_e64 v8, v240, v146, s[6:7]
	s_and_b64 s[36:37], s[40:41], s[36:37]
	s_movk_i32 s34, 0xffc6
	v_cndmask_b32_e64 v146, v146, v8, s[36:37]
	v_cndmask_b32_e64 v148, v148, v240, s[36:37]
	v_cndmask_b32_e64 v147, v147, v7, s[36:37]
	s_movk_i32 s36, 0xffc5
	s_movk_i32 s30, 0xffc7
	v_cmp_lt_i32_e64 s[34:35], s34, v2
	v_cmp_lt_i32_e64 s[36:37], s36, v2
	s_movk_i32 s28, 0xffc8
	v_cmp_lt_i32_e64 s[30:31], s30, v2
	s_and_b64 s[34:35], s[36:37], s[34:35]
	s_movk_i32 s26, 0xffcd
	v_cmp_lt_i32_e64 s[28:29], s28, v2
	s_and_b64 s[30:31], s[34:35], s[30:31]
	s_movk_i32 s24, 0xffce
	v_cmp_lt_i32_e64 s[26:27], s26, v2
	s_and_b64 s[28:29], s[30:31], s[28:29]
	s_movk_i32 s22, 0xffcf
	v_cmp_lt_i32_e64 s[24:25], s24, v2
	s_and_b64 s[26:27], s[28:29], s[26:27]
	s_movk_i32 s20, 0xffd0
	v_cmp_lt_i32_e64 s[22:23], s22, v2
	s_and_b64 s[24:25], s[26:27], s[24:25]
	s_movk_i32 s18, 0xffd5
	v_cmp_lt_i32_e64 s[20:21], s20, v2
	s_and_b64 s[22:23], s[24:25], s[22:23]
	s_movk_i32 s16, 0xffd6
	v_cmp_lt_i32_e64 s[18:19], s18, v2
	s_and_b64 s[20:21], s[22:23], s[20:21]
	s_movk_i32 s14, 0xffd7
	v_cmp_lt_i32_e64 s[16:17], s16, v2
	s_and_b64 s[18:19], s[20:21], s[18:19]
	s_movk_i32 s12, 0xffd8
	v_cmp_lt_i32_e64 s[14:15], s14, v2
	s_and_b64 s[16:17], s[18:19], s[16:17]
	s_movk_i32 s10, 0xffdd
	v_cmp_lt_i32_e64 s[12:13], s12, v2
	s_and_b64 s[14:15], s[16:17], s[14:15]
	s_movk_i32 s8, 0xffde
	v_cmp_lt_i32_e64 s[10:11], s10, v2
	s_and_b64 s[12:13], s[14:15], s[12:13]
	s_movk_i32 s6, 0xffdf
	v_cmp_lt_i32_e64 s[8:9], s8, v2
	s_and_b64 s[10:11], s[12:13], s[10:11]
	v_cmp_lt_i32_e64 s[6:7], s6, v2
	s_and_b64 s[8:9], s[10:11], s[8:9]
	s_and_b64 s[6:7], s[8:9], s[6:7]
	v_cndmask_b32_e64 v154, v154, v240, s[50:51]
	s_mov_b32 s50, 0x42000000
	v_cndmask_b32_e64 v153, v153, v240, s[48:49]
	s_mov_b32 s48, 0x42080000
	v_cndmask_b32_e64 v152, v152, v240, s[46:47]
	s_mov_b32 s46, 0x42200000
	v_cndmask_b32_e64 v150, v150, v240, s[42:43]
	s_mov_b32 s42, 0x42280000
	v_cndmask_b32_e64 v149, v149, v240, s[40:41]
	s_mov_b32 s40, 0x42400000
	v_cndmask_b32_e64 v177, v177, v240, s[36:37]
	s_mov_b32 s36, 0x42480000
	v_cndmask_b32_e64 v176, v176, v240, s[34:35]
	s_mov_b32 s34, 0x42600000
	v_cndmask_b32_e64 v175, v175, v240, s[30:31]
	s_mov_b32 s30, 0x42680000
	v_cndmask_b32_e64 v174, v174, v240, s[28:29]
	s_mov_b32 s28, 0x41d00000
	v_cndmask_b32_e64 v173, v173, v240, s[26:27]
	s_mov_b32 s26, 0x41c00000
	v_cndmask_b32_e64 v172, v172, v240, s[24:25]
	s_mov_b32 s24, 0x41900000
	v_cndmask_b32_e64 v171, v171, v240, s[22:23]
	s_mov_b32 s22, 0x41800000
	v_cndmask_b32_e64 v170, v170, v240, s[20:21]
	s_mov_b32 s20, 0x41200000
	v_cndmask_b32_e64 v169, v169, v240, s[18:19]
	s_mov_b32 s18, 0x41000000
	v_cndmask_b32_e64 v168, v168, v240, s[16:17]
	s_mov_b32 s16, 2.0
	s_and_b64 vcc, s[6:7], vcc
	v_cndmask_b32_e64 v161, v161, v240, s[64:65]
	v_cndmask_b32_e64 v160, v160, v240, s[62:63]
	v_cndmask_b32_e64 v159, v159, v240, s[60:61]
	v_cndmask_b32_e64 v158, v158, v240, s[58:59]
	v_cndmask_b32_e64 v157, v157, v240, s[56:57]
	v_cndmask_b32_e64 v156, v156, v240, s[54:55]
	v_cndmask_b32_e64 v155, v155, v240, s[52:53]
	s_mov_b32 s51, 0x42040000
	s_mov_b32 s49, 0x420c0000
	s_mov_b32 s47, 0x42240000
	v_cndmask_b32_e64 v151, v151, v240, s[44:45]
	s_movk_i32 s45, 0x70
	s_mov_b32 s43, 0x422c0000
	s_mov_b32 s41, 0x42440000
	s_mov_b32 s37, 0x424c0000
	s_mov_b32 s35, 0x42640000
	s_mov_b32 s31, 0x426c0000
	s_mov_b32 s29, 0x41d80000
	s_mov_b32 s27, 0x41c80000
	s_mov_b32 s25, 0x41980000
	s_mov_b32 s23, 0x41880000
	s_mov_b32 s21, 0x41300000
	s_mov_b32 s19, 0x41100000
	s_mov_b32 s17, 0x40400000
	v_cndmask_b32_e64 v167, v167, v240, s[14:15]
	v_cndmask_b32_e64 v166, v166, v240, s[12:13]
	v_cndmask_b32_e64 v165, v165, v240, s[10:11]
	v_cndmask_b32_e64 v164, v164, v240, s[8:9]
	v_cndmask_b32_e64 v163, v163, v240, s[6:7]
	v_cndmask_b32_e32 v162, v162, v240, vcc
